# helper workgroups with item ranges scaled by the number of busy XCD groups (512 items per busy group after E1, 256 after E2, rest on the lightly loaded groups)
# speedup vs baseline: 1.0105x; 1.0105x over previous
;     __device__ bool next(int i, Unit& u) const {
;         const long L = (long)i * G + c; int wgid;
;         if (aligned) {
;             const int ng = (nM + WGM - 1) / WGM, gq = ng / NXCD, gr = ng % NXCD, xcd = (int)(L % NXCD); const long off = L / NXCD;
;             const int g0 = xcd * gq + (xcd < gr ? xcd : gr), g1 = g0 + gq + (xcd < gr ? 1 : 0);
;             const long w = (long)g0 * (WGM * 4) + off, wend = (long)g1 * (WGM * 4) < nwg ? (long)g1 * (WGM * 4) : nwg;
;             if (w >= wend) return false;
;             wgid = (int)w;
; __global__ void __launch_bounds__(NWAVES * 64, 2) mk_fwd(Args args) {
;     ...
;         {
;             const int step = G * NWAVES; int it0 = CONV_EARLY + bid * NWAVES + wave;
;             ConvDesc dA, dB; f32x4 vA[16], vB[16];
;             if (it0 < NCONV_ITEMS) { CONV_DECODE(dA, it0); conv_load(vA, dA, lane); }
; #pragma unroll 1
;             for (; it0 < NCONV_ITEMS; it0 += 2 * step) {
;                 const bool hasB = it0 + step < NCONV_ITEMS, hasA2 = it0 + 2 * step < NCONV_ITEMS;
;                 if (hasB) { CONV_DECODE(dB, it0 + step); conv_load(vB, dB, lane); }
;                 conv_process(vA, dA, scr, lane);
;                 if (hasA2) { CONV_DECODE(dA, it0 + 2 * step); conv_load(vA, dA, lane); }
;                 if (hasB) conv_process(vB, dB, scr, lane);
;             }
.LBB0_1541:
	v_mov_b32_e32 v252, 0x27c80
	ds_read_b32 v252, v252
	s_waitcnt lgkmcnt(0)
	v_readfirstlane_b32 s100, v252
	s_nop 1
	s_lshr_b32 s100, s100, 8
	s_add_i32 s100, s100, 3
	s_lshr_b32 s100, s100, 2
	s_and_b32 s100, s100, 7
	s_cmp_eq_u32 s100, 0
	s_cbranch_scc1 .LslotA_skip
	s_cmp_ge_u32 s100, 6
	s_cbranch_scc1 .LslotA_skip
	s_and_b32 s98, s83, 7
	s_cmp_ge_u32 s98, s100
	s_cbranch_scc1 .LslotA_skip
	s_lshr_b32 s101, s83, 3
	s_cmp_lt_u32 s101, 16
	s_cbranch_scc1 .LslotA_skip
	s_lshl_b32 s98, s98, 4
	s_add_i32 s98, s98, s101
	s_sub_i32 s98, s98, 16
	s_lshl_b32 s100, s100, 4
	s_add_i32 s98, s98, 0x600
	v_writelane_b32 v253, s14, 0
	v_writelane_b32 v253, s15, 1
	v_writelane_b32 v253, s16, 2
	v_writelane_b32 v253, s17, 3
	v_writelane_b32 v253, s19, 4
	v_writelane_b32 v253, s21, 5
	v_writelane_b32 v253, s57, 6
	v_mov_b32_e32 v254, v3
	s_mov_b32 s99, 5
	s_lshl_b32 s101, s100, 5
	s_add_i32 s101, s101, 0x3900
	s_lshl_b32 s50, s98, 3
	s_add_i32 s50, s50, s85
	s_lshl_b32 s49, s98, 9
	s_lshl_b32 s48, s100, 3
	s_lshl_b32 s2, s100, 9
	s_mov_b64 s[0:1], s[78:79]
	s_mul_i32 s3, s85, 0x4100
	s_lshl_b32 s88, s85, 6
	s_branch .Lconv_entry

;     __device__ bool next(int i, Unit& u) const {
;         const long L = (long)i * G + c; int wgid;
;         if (aligned) {
;             const int ng = (nM + WGM - 1) / WGM, gq = ng / NXCD, gr = ng % NXCD, xcd = (int)(L % NXCD); const long off = L / NXCD;
;             const int g0 = xcd * gq + (xcd < gr ? xcd : gr), g1 = g0 + gq + (xcd < gr ? 1 : 0);
;             const long w = (long)g0 * (WGM * 4) + off, wend = (long)g1 * (WGM * 4) < nwg ? (long)g1 * (WGM * 4) : nwg;
;             if (w >= wend) return false;
;             wgid = (int)w;
; __global__ void __launch_bounds__(NWAVES * 64, 2) mk_fwd(Args args) {
;     ...
;         {
;             const int step = G * NWAVES; int it0 = CONV_EARLY + bid * NWAVES + wave;
;             ConvDesc dA, dB; f32x4 vA[16], vB[16];
;             if (it0 < NCONV_ITEMS) { CONV_DECODE(dA, it0); conv_load(vA, dA, lane); }
; #pragma unroll 1
;             for (; it0 < NCONV_ITEMS; it0 += 2 * step) {
;                 const bool hasB = it0 + step < NCONV_ITEMS, hasA2 = it0 + 2 * step < NCONV_ITEMS;
;                 if (hasB) { CONV_DECODE(dB, it0 + step); conv_load(vB, dB, lane); }
;                 conv_process(vA, dA, scr, lane);
;                 if (hasA2) { CONV_DECODE(dA, it0 + 2 * step); conv_load(vA, dA, lane); }
;                 if (hasB) conv_process(vB, dB, scr, lane);
;             }
.LBB0_1657:
	s_waitcnt vmcnt(0) lgkmcnt(0)
	s_barrier
	v_mov_b32_e32 v252, 0x27c80
	ds_read_b32 v252, v252
	s_waitcnt lgkmcnt(0)
	v_readfirstlane_b32 s100, v252
	s_nop 1
	s_lshr_b32 s100, s100, 8
	s_add_i32 s100, s100, 3
	s_lshr_b32 s100, s100, 2
	s_and_b32 s100, s100, 7
	s_and_b32 s98, s83, 7
	s_cmp_eq_u32 s100, 0
	s_cbranch_scc1 .Lsp_all
	s_cmp_ge_u32 s100, 6
	s_cbranch_scc1 .Lsp_all
	s_lshr_b32 s101, s83, 3
	s_cmp_lt_u32 s98, s100
	s_cbranch_scc1 .Lsp_heavy
	s_sub_i32 s98, s98, s100
	s_lshl_b32 s98, s98, 5
	s_add_i32 s98, s98, s101
	s_lshl_b32 s101, s100, 6
	s_add_i32 s98, s98, s101
	s_lshl_b32 s101, s100, 5
	s_add_i32 s98, s98, s101
	s_sub_i32 s100, 8, s100
	s_lshl_b32 s100, s100, 5
	s_add_i32 s98, s98, 0x600
	s_branch .Lsp_go
.Lsp_heavy:
	s_cmp_lt_u32 s101, 16
	s_cbranch_scc1 .Lq_done
	s_lshl_b32 s98, s98, 4
	s_add_i32 s98, s98, s101
	s_sub_i32 s98, s98, 16
	s_lshl_b32 s100, s100, 4
	s_lshl_b32 s101, s100, 2
	s_add_i32 s98, s98, s101
	s_add_i32 s98, s98, 0x600
	s_lshl_b32 s101, s100, 5
	s_lshl_b32 s99, s100, 4
	s_add_i32 s101, s101, s99
	s_add_i32 s101, s101, 0x3900
	s_mov_b32 s99, 2
	s_lshl_b32 s50, s98, 3
	s_add_i32 s50, s50, s85
	s_lshl_b32 s49, s98, 9
	s_lshl_b32 s48, s100, 3
	s_lshl_b32 s2, s100, 9
	s_mov_b64 s[0:1], s[78:79]
	s_mul_i32 s3, s85, 0x4100
	s_lshl_b32 s88, s85, 6
	s_branch .Lconv_entry
